# nt hint also on the merge epilogue's read-once gate loads and the in-projection output stores
# baseline (speedup 1.0000x reference)
.LBB0_269:
	s_andn2_b64 vcc, exec, s[50:51]
	v_readlane_b32 s36, v255, 12
	v_readlane_b32 s83, v255, 13
	s_mov_b32 s37, s8
	s_cbranch_vccnz .LBB0_271
	s_ashr_i32 s28, s65, 2
	s_andn2_b32 s28, s28, 63
	s_lshl_b32 s29, s86, 8
	s_add_i32 s28, s28, s29
	v_or_b32_e32 v130, s28, v155
	v_ashrrev_i32_e32 v131, 31, v130
	v_lshlrev_b64 v[130:131], 9, v[130:131]
	v_lshl_add_u64 v[130:131], s[76:77], 0, v[130:131]
	s_lshl_b32 s28, s71, 1
	s_mov_b32 s29, s5
	v_lshl_add_u64 v[130:131], v[130:131], 0, s[28:29]
	v_lshlrev_b32_e32 v112, 1, v112
	v_lshl_add_u64 v[130:131], v[130:131], 0, v[112:113]
	v_cvt_pk_bf16_f32 v108, v108, v109
	v_cvt_pk_bf16_f32 v109, v110, v111
	v_cvt_pk_bf16_f32 v110, v104, v105
	v_cvt_pk_bf16_f32 v111, v106, v107
	global_store_dwordx4 v[130:131], v[108:111], off offset:256 nt
	v_cvt_pk_bf16_f32 v92, v92, v93
	v_cvt_pk_bf16_f32 v93, v94, v95
	v_add_co_u32_e32 v108, vcc, s59, v130
	v_cvt_pk_bf16_f32 v94, v88, v89
	s_nop 0
	v_addc_co_u32_e32 v109, vcc, 0, v131, vcc
	v_cvt_pk_bf16_f32 v95, v90, v91
	global_store_dwordx4 v[108:109], v[92:95], off offset:256 nt
	v_cvt_pk_bf16_f32 v76, v76, v77
	v_cvt_pk_bf16_f32 v77, v78, v79
	v_add_co_u32_e32 v92, vcc, s62, v130
	v_cvt_pk_bf16_f32 v78, v72, v73
	s_nop 0
	v_addc_co_u32_e32 v93, vcc, 0, v131, vcc
	v_cvt_pk_bf16_f32 v79, v74, v75
	global_store_dwordx4 v[92:93], v[76:79], off offset:256 nt
	v_cvt_pk_bf16_f32 v60, v60, v61
	v_cvt_pk_bf16_f32 v61, v62, v63
	v_add_co_u32_e32 v76, vcc, s89, v130
	v_cvt_pk_bf16_f32 v62, v56, v57
	s_nop 0
	v_addc_co_u32_e32 v77, vcc, 0, v131, vcc
	v_add_co_u32_e32 v56, vcc, s63, v130
	v_cvt_pk_bf16_f32 v44, v44, v45
	s_nop 0
	v_addc_co_u32_e32 v57, vcc, 0, v131, vcc
	v_cvt_pk_bf16_f32 v45, v46, v47
	v_cvt_pk_bf16_f32 v46, v40, v41
	v_cvt_pk_bf16_f32 v47, v42, v43
	s_mov_b32 s28, 0x12000
	global_store_dwordx4 v[56:57], v[44:47], off offset:256 nt
	v_cvt_pk_bf16_f32 v28, v28, v29
	v_cvt_pk_bf16_f32 v29, v30, v31
	v_add_co_u32_e32 v44, vcc, s28, v130
	v_cvt_pk_bf16_f32 v30, v24, v25
	s_nop 0
	v_addc_co_u32_e32 v45, vcc, 0, v131, vcc
	v_cvt_pk_bf16_f32 v31, v26, v27
	s_mov_b32 s28, 0x14000
	global_store_dwordx4 v[44:45], v[28:31], off offset:256 nt
	v_cvt_pk_bf16_f32 v12, v12, v13
	v_cvt_pk_bf16_f32 v13, v14, v15
	v_add_co_u32_e32 v28, vcc, s28, v130
	v_cvt_pk_bf16_f32 v14, v8, v9
	s_nop 0
	v_addc_co_u32_e32 v29, vcc, 0, v131, vcc
	v_cvt_pk_bf16_f32 v15, v10, v11
	s_mov_b32 s28, 0x16000
	global_store_dwordx4 v[28:29], v[12:15], off offset:256 nt
	v_cvt_pk_bf16_f32 v126, v126, v127
	v_cvt_pk_bf16_f32 v127, v128, v129
	v_add_co_u32_e32 v12, vcc, s28, v130
	v_cvt_pk_bf16_f32 v128, v122, v123
	v_cvt_pk_bf16_f32 v129, v124, v125
	v_cvt_pk_bf16_f32 v104, v118, v119
	v_cvt_pk_bf16_f32 v105, v120, v121
	v_cvt_pk_bf16_f32 v106, v114, v115
	v_cvt_pk_bf16_f32 v107, v116, v117
	v_cvt_pk_bf16_f32 v88, v100, v101
	v_cvt_pk_bf16_f32 v89, v102, v103
	v_cvt_pk_bf16_f32 v90, v96, v97
	v_cvt_pk_bf16_f32 v91, v98, v99
	v_cvt_pk_bf16_f32 v72, v84, v85
	v_cvt_pk_bf16_f32 v73, v86, v87
	v_cvt_pk_bf16_f32 v74, v80, v81
	v_cvt_pk_bf16_f32 v75, v82, v83
	v_cvt_pk_bf16_f32 v68, v68, v69
	v_cvt_pk_bf16_f32 v69, v70, v71
	v_cvt_pk_bf16_f32 v70, v64, v65
	v_cvt_pk_bf16_f32 v71, v66, v67
	v_cvt_pk_bf16_f32 v63, v58, v59
	v_cvt_pk_bf16_f32 v40, v52, v53
	v_cvt_pk_bf16_f32 v41, v54, v55
	v_cvt_pk_bf16_f32 v42, v48, v49
	v_cvt_pk_bf16_f32 v43, v50, v51
	v_cvt_pk_bf16_f32 v24, v36, v37
	v_cvt_pk_bf16_f32 v25, v38, v39
	v_cvt_pk_bf16_f32 v26, v32, v33
	v_cvt_pk_bf16_f32 v27, v34, v35
	v_cvt_pk_bf16_f32 v8, v20, v21
	v_cvt_pk_bf16_f32 v9, v22, v23
	v_cvt_pk_bf16_f32 v10, v16, v17
	v_cvt_pk_bf16_f32 v11, v18, v19
	v_addc_co_u32_e32 v13, vcc, 0, v131, vcc
	v_cvt_pk_bf16_f32 v4, v4, v5
	v_cvt_pk_bf16_f32 v5, v6, v7
	v_cvt_pk_bf16_f32 v6, v0, v1
	v_cvt_pk_bf16_f32 v7, v2, v3
	global_store_dwordx4 v[130:131], v[126:129], off nt
	global_store_dwordx4 v[108:109], v[104:107], off nt
	global_store_dwordx4 v[92:93], v[88:91], off nt
	global_store_dwordx4 v[76:77], v[72:75], off nt
	global_store_dwordx4 v[76:77], v[68:71], off offset:256 nt
	global_store_dwordx4 v[56:57], v[60:63], off nt
	global_store_dwordx4 v[44:45], v[40:43], off nt
	global_store_dwordx4 v[28:29], v[24:27], off nt
	global_store_dwordx4 v[12:13], v[8:11], off nt
	global_store_dwordx4 v[12:13], v[4:7], off offset:256 nt

.LBB0_764:
	global_load_dwordx4 v[160:163], v[114:115], off nt
	s_ashr_i32 s28, s28, 2
	s_lshl_b32 s29, s74, 8
	s_andn2_b32 s28, s28, 63
	s_add_i32 s28, s28, s29
	v_or_b32_e32 v172, s28, v132
	v_add_co_u32_e32 v132, vcc, 0x2000, v114
	s_mov_b32 s31, 0x8000
	s_nop 0
	v_addc_co_u32_e32 v133, vcc, 0, v115, vcc
	global_load_dwordx4 v[156:159], v[132:133], off nt
	v_add_co_u32_e32 v132, vcc, 0x4000, v114
	s_mov_b32 s24, 0xa000
	s_nop 0
	v_addc_co_u32_e32 v133, vcc, 0, v115, vcc
	global_load_dwordx4 v[152:155], v[132:133], off nt
	v_add_co_u32_e32 v132, vcc, s89, v114
	v_ashrrev_i32_e32 v173, 31, v172
	s_nop 0
	v_addc_co_u32_e32 v133, vcc, 0, v115, vcc
	global_load_dwordx4 v[148:151], v[132:133], off nt
	v_add_co_u32_e32 v132, vcc, s31, v114
	v_lshlrev_b64 v[172:173], 11, v[172:173]
	s_nop 0
	v_addc_co_u32_e32 v133, vcc, 0, v115, vcc
	global_load_dwordx4 v[144:147], v[132:133], off nt
	v_add_co_u32_e32 v132, vcc, s24, v114
	s_lshl_b32 s28, s6, 8
	s_nop 0
	v_addc_co_u32_e32 v133, vcc, 0, v115, vcc
	global_load_dwordx4 v[140:143], v[132:133], off nt
	s_mov_b32 s24, 0xc000
	v_lshl_add_u64 v[172:173], s[10:11], 0, v[172:173]
	s_ashr_i32 s29, s28, 31
	v_add_co_u32_e32 v132, vcc, s24, v114
	v_lshl_add_u64 v[172:173], s[28:29], 1, v[172:173]
	s_mov_b32 s28, 0x3b808081
	v_addc_co_u32_e32 v133, vcc, 0, v115, vcc
	s_mov_b32 s24, 0xe000
	global_load_dwordx4 v[136:139], v[132:133], off nt
	v_add_co_u32_e32 v132, vcc, s24, v114
	v_lshl_or_b32 v112, s7, 6, v112
	s_nop 0
	v_addc_co_u32_e32 v133, vcc, 0, v115, vcc
	v_lshl_add_u64 v[172:173], v[172:173], 0, v[112:113]
	global_load_dwordx4 v[132:135], v[132:133], off nt
	s_mov_b32 s7, 0x18000
	s_mov_b32 s24, 0x8000
	s_waitcnt vmcnt(0)
	v_cvt_f32_ubyte1_e32 v179, v160
	v_cvt_f32_ubyte0_e32 v178, v160
	v_cvt_f32_ubyte1_e32 v181, v161
	v_cvt_f32_ubyte0_e32 v180, v161
	v_cvt_f32_ubyte3_e32 v183, v160
	v_cvt_f32_ubyte2_e32 v182, v160
	v_cvt_f32_ubyte3_e32 v185, v161
	v_cvt_f32_ubyte2_e32 v184, v161
	v_pk_mul_f32 v[178:179], v[178:179], s[28:29] op_sel_hi:[1,0]
	v_pk_mul_f32 v[180:181], v[180:181], s[28:29] op_sel_hi:[1,0]
	v_pk_mul_f32 v[182:183], v[182:183], s[28:29] op_sel_hi:[1,0]
	v_pk_mul_f32 v[160:161], v[184:185], s[28:29] op_sel_hi:[1,0]
	v_pk_mul_f32 v[178:179], v[128:129], v[178:179]
	v_pk_mul_f32 v[180:181], v[124:125], v[180:181]
	v_pk_mul_f32 v[182:183], v[130:131], v[182:183]
	v_pk_mul_f32 v[160:161], v[126:127], v[160:161]
	v_cvt_pk_bf16_f32 v178, v178, v179
	v_cvt_pk_bf16_f32 v179, v182, v183
	v_cvt_pk_bf16_f32 v180, v180, v181
	v_cvt_pk_bf16_f32 v181, v160, v161
	global_store_dwordx4 v[172:173], v[178:181], off
	v_cvt_f32_ubyte1_e32 v161, v162
	v_cvt_f32_ubyte0_e32 v160, v162
	v_cvt_f32_ubyte1_e32 v179, v163
	v_cvt_f32_ubyte0_e32 v178, v163
	v_pk_mul_f32 v[178:179], v[178:179], s[28:29] op_sel_hi:[1,0]
	v_pk_mul_f32 v[160:161], v[160:161], s[28:29] op_sel_hi:[1,0]
	v_pk_mul_f32 v[180:181], v[116:117], v[178:179]
	v_cvt_f32_ubyte3_e32 v179, v162
	v_cvt_f32_ubyte2_e32 v178, v162
	v_pk_mul_f32 v[178:179], v[178:179], s[28:29] op_sel_hi:[1,0]
	v_pk_mul_f32 v[160:161], v[120:121], v[160:161]
	v_pk_mul_f32 v[182:183], v[122:123], v[178:179]
	v_cvt_f32_ubyte3_e32 v179, v163
	v_cvt_f32_ubyte2_e32 v178, v163
	v_pk_mul_f32 v[162:163], v[178:179], s[28:29] op_sel_hi:[1,0]
	v_cvt_pk_bf16_f32 v178, v160, v161
	v_pk_mul_f32 v[162:163], v[118:119], v[162:163]
	v_add_co_u32_e32 v160, vcc, s31, v172
	v_cvt_pk_bf16_f32 v179, v182, v183
	v_cvt_pk_bf16_f32 v180, v180, v181
	v_cvt_pk_bf16_f32 v181, v162, v163
	v_addc_co_u32_e32 v161, vcc, 0, v173, vcc
	global_store_dwordx4 v[160:161], v[178:181], off
	v_cvt_f32_ubyte1_e32 v163, v156
	v_cvt_f32_ubyte0_e32 v162, v156
	v_cvt_f32_ubyte1_e32 v179, v157
	v_cvt_f32_ubyte0_e32 v178, v157
	v_pk_mul_f32 v[178:179], v[178:179], s[28:29] op_sel_hi:[1,0]
	v_pk_mul_f32 v[162:163], v[162:163], s[28:29] op_sel_hi:[1,0]
	v_pk_mul_f32 v[180:181], v[104:105], v[178:179]
	v_cvt_f32_ubyte3_e32 v179, v156
	v_cvt_f32_ubyte2_e32 v178, v156
	v_pk_mul_f32 v[178:179], v[178:179], s[28:29] op_sel_hi:[1,0]
	v_pk_mul_f32 v[162:163], v[108:109], v[162:163]
	v_pk_mul_f32 v[182:183], v[110:111], v[178:179]
	v_cvt_f32_ubyte3_e32 v179, v157
	v_cvt_f32_ubyte2_e32 v178, v157
	v_pk_mul_f32 v[156:157], v[178:179], s[28:29] op_sel_hi:[1,0]
	v_cvt_pk_bf16_f32 v180, v180, v181
	v_pk_mul_f32 v[156:157], v[106:107], v[156:157]
	v_cvt_pk_bf16_f32 v178, v162, v163
	v_cvt_pk_bf16_f32 v181, v156, v157
	v_add_co_u32_e32 v156, vcc, s30, v172
	v_cvt_pk_bf16_f32 v179, v182, v183
	s_nop 0
	v_addc_co_u32_e32 v157, vcc, 0, v173, vcc
	global_store_dwordx4 v[156:157], v[178:181], off
	v_cvt_f32_ubyte1_e32 v163, v158
	v_cvt_f32_ubyte0_e32 v162, v158
	v_cvt_f32_ubyte1_e32 v179, v159
	v_cvt_f32_ubyte0_e32 v178, v159
	v_pk_mul_f32 v[178:179], v[178:179], s[28:29] op_sel_hi:[1,0]
	v_pk_mul_f32 v[162:163], v[162:163], s[28:29] op_sel_hi:[1,0]
	v_pk_mul_f32 v[180:181], v[96:97], v[178:179]
	v_cvt_f32_ubyte3_e32 v179, v158
	v_cvt_f32_ubyte2_e32 v178, v158
	v_pk_mul_f32 v[178:179], v[178:179], s[28:29] op_sel_hi:[1,0]
	v_pk_mul_f32 v[162:163], v[100:101], v[162:163]
	v_pk_mul_f32 v[182:183], v[102:103], v[178:179]
	v_cvt_f32_ubyte3_e32 v179, v159
	v_cvt_f32_ubyte2_e32 v178, v159
	v_pk_mul_f32 v[158:159], v[178:179], s[28:29] op_sel_hi:[1,0]
	v_cvt_pk_bf16_f32 v180, v180, v181
	v_pk_mul_f32 v[158:159], v[98:99], v[158:159]
	v_cvt_pk_bf16_f32 v178, v162, v163
	v_cvt_pk_bf16_f32 v181, v158, v159
	v_add_co_u32_e32 v158, vcc, s7, v172
	v_cvt_pk_bf16_f32 v179, v182, v183
	s_nop 0
	v_addc_co_u32_e32 v159, vcc, 0, v173, vcc
	global_store_dwordx4 v[158:159], v[178:181], off
	v_cvt_f32_ubyte1_e32 v163, v152
	v_cvt_f32_ubyte0_e32 v162, v152
	v_cvt_f32_ubyte1_e32 v179, v153
	v_cvt_f32_ubyte0_e32 v178, v153
	v_pk_mul_f32 v[178:179], v[178:179], s[28:29] op_sel_hi:[1,0]
	v_pk_mul_f32 v[162:163], v[162:163], s[28:29] op_sel_hi:[1,0]
	v_pk_mul_f32 v[180:181], v[56:57], v[178:179]
	v_cvt_f32_ubyte3_e32 v179, v152
	v_cvt_f32_ubyte2_e32 v178, v152
	v_pk_mul_f32 v[178:179], v[178:179], s[28:29] op_sel_hi:[1,0]
	s_mov_b32 s7, 0x40000
	v_pk_mul_f32 v[182:183], v[62:63], v[178:179]
	v_cvt_f32_ubyte3_e32 v179, v153
	v_cvt_f32_ubyte2_e32 v178, v153
	v_pk_mul_f32 v[152:153], v[178:179], s[28:29] op_sel_hi:[1,0]
	v_pk_mul_f32 v[162:163], v[60:61], v[162:163]
	v_pk_mul_f32 v[152:153], v[58:59], v[152:153]
	v_cvt_pk_bf16_f32 v180, v180, v181
	v_cvt_pk_bf16_f32 v181, v152, v153
	v_add_co_u32_e32 v152, vcc, s7, v172
	v_cvt_pk_bf16_f32 v178, v162, v163
	v_cvt_pk_bf16_f32 v179, v182, v183
	v_addc_co_u32_e32 v153, vcc, 0, v173, vcc
	global_store_dwordx4 v[152:153], v[178:181], off
	v_cvt_f32_ubyte1_e32 v163, v154
	v_cvt_f32_ubyte0_e32 v162, v154
	v_cvt_f32_ubyte1_e32 v179, v155
	v_cvt_f32_ubyte0_e32 v178, v155
	v_pk_mul_f32 v[178:179], v[178:179], s[28:29] op_sel_hi:[1,0]
	v_pk_mul_f32 v[162:163], v[162:163], s[28:29] op_sel_hi:[1,0]
	v_pk_mul_f32 v[180:181], v[48:49], v[178:179]
	v_cvt_f32_ubyte3_e32 v179, v154
	v_cvt_f32_ubyte2_e32 v178, v154
	v_pk_mul_f32 v[178:179], v[178:179], s[28:29] op_sel_hi:[1,0]
	s_mov_b32 s7, 0x48000
	v_pk_mul_f32 v[182:183], v[54:55], v[178:179]
	v_cvt_f32_ubyte3_e32 v179, v155
	v_cvt_f32_ubyte2_e32 v178, v155
	v_pk_mul_f32 v[154:155], v[178:179], s[28:29] op_sel_hi:[1,0]
	v_pk_mul_f32 v[162:163], v[52:53], v[162:163]
	v_pk_mul_f32 v[154:155], v[50:51], v[154:155]
	v_cvt_pk_bf16_f32 v180, v180, v181
	v_cvt_pk_bf16_f32 v181, v154, v155
	v_add_co_u32_e32 v154, vcc, s7, v172
	v_cvt_pk_bf16_f32 v178, v162, v163
	v_cvt_pk_bf16_f32 v179, v182, v183
	v_addc_co_u32_e32 v155, vcc, 0, v173, vcc
	global_store_dwordx4 v[154:155], v[178:181], off
	v_cvt_f32_ubyte1_e32 v163, v148
	v_cvt_f32_ubyte0_e32 v162, v148
	v_cvt_f32_ubyte1_e32 v179, v149
	v_cvt_f32_ubyte0_e32 v178, v149
	v_pk_mul_f32 v[178:179], v[178:179], s[28:29] op_sel_hi:[1,0]
	v_pk_mul_f32 v[162:163], v[162:163], s[28:29] op_sel_hi:[1,0]
	v_pk_mul_f32 v[180:181], v[40:41], v[178:179]
	v_cvt_f32_ubyte3_e32 v179, v148
	v_cvt_f32_ubyte2_e32 v178, v148
	v_pk_mul_f32 v[178:179], v[178:179], s[28:29] op_sel_hi:[1,0]
	s_mov_b32 s7, 0x50000
	v_pk_mul_f32 v[182:183], v[46:47], v[178:179]
	v_cvt_f32_ubyte3_e32 v179, v149
	v_cvt_f32_ubyte2_e32 v178, v149
	v_pk_mul_f32 v[148:149], v[178:179], s[28:29] op_sel_hi:[1,0]
	v_pk_mul_f32 v[162:163], v[44:45], v[162:163]
	v_pk_mul_f32 v[148:149], v[42:43], v[148:149]
	v_cvt_pk_bf16_f32 v180, v180, v181
	v_cvt_pk_bf16_f32 v181, v148, v149
	v_add_co_u32_e32 v148, vcc, s7, v172
	v_cvt_pk_bf16_f32 v178, v162, v163
	v_cvt_pk_bf16_f32 v179, v182, v183
	v_addc_co_u32_e32 v149, vcc, 0, v173, vcc
	global_store_dwordx4 v[148:149], v[178:181], off
	v_cvt_f32_ubyte1_e32 v163, v150
	v_cvt_f32_ubyte0_e32 v162, v150
	v_cvt_f32_ubyte1_e32 v179, v151
	v_cvt_f32_ubyte0_e32 v178, v151
	v_pk_mul_f32 v[178:179], v[178:179], s[28:29] op_sel_hi:[1,0]
	v_pk_mul_f32 v[162:163], v[162:163], s[28:29] op_sel_hi:[1,0]
	v_pk_mul_f32 v[180:181], v[32:33], v[178:179]
	v_cvt_f32_ubyte3_e32 v179, v150
	v_cvt_f32_ubyte2_e32 v178, v150
	v_pk_mul_f32 v[178:179], v[178:179], s[28:29] op_sel_hi:[1,0]
	s_mov_b32 s7, 0x58000
	v_pk_mul_f32 v[182:183], v[38:39], v[178:179]
	v_cvt_f32_ubyte3_e32 v179, v151
	v_cvt_f32_ubyte2_e32 v178, v151
	v_pk_mul_f32 v[150:151], v[178:179], s[28:29] op_sel_hi:[1,0]
	v_pk_mul_f32 v[162:163], v[36:37], v[162:163]
	v_pk_mul_f32 v[150:151], v[34:35], v[150:151]
	v_cvt_pk_bf16_f32 v180, v180, v181
	v_cvt_pk_bf16_f32 v181, v150, v151
	v_add_co_u32_e32 v150, vcc, s7, v172
	v_cvt_pk_bf16_f32 v178, v162, v163
	v_cvt_pk_bf16_f32 v179, v182, v183
	v_addc_co_u32_e32 v151, vcc, 0, v173, vcc
	global_store_dwordx4 v[150:151], v[178:181], off
	v_cvt_f32_ubyte1_e32 v163, v144
	v_cvt_f32_ubyte0_e32 v162, v144
	v_cvt_f32_ubyte1_e32 v179, v145
	v_cvt_f32_ubyte0_e32 v178, v145
	v_pk_mul_f32 v[178:179], v[178:179], s[28:29] op_sel_hi:[1,0]
	v_pk_mul_f32 v[162:163], v[162:163], s[28:29] op_sel_hi:[1,0]
	v_pk_mul_f32 v[180:181], v[88:89], v[178:179]
	v_cvt_f32_ubyte3_e32 v179, v144
	v_cvt_f32_ubyte2_e32 v178, v144
	v_pk_mul_f32 v[178:179], v[178:179], s[28:29] op_sel_hi:[1,0]
	v_pk_mul_f32 v[162:163], v[92:93], v[162:163]
	v_pk_mul_f32 v[182:183], v[94:95], v[178:179]
	v_cvt_f32_ubyte3_e32 v179, v145
	v_cvt_f32_ubyte2_e32 v178, v145
	v_pk_mul_f32 v[144:145], v[178:179], s[28:29] op_sel_hi:[1,0]
	v_cvt_pk_bf16_f32 v178, v162, v163
	v_pk_mul_f32 v[144:145], v[90:91], v[144:145]
	v_cvt_pk_bf16_f32 v179, v182, v183
	v_cvt_pk_bf16_f32 v180, v180, v181
	v_cvt_pk_bf16_f32 v181, v144, v145
	global_store_dwordx4 v[172:173], v[178:181], off offset:256
	v_cvt_f32_ubyte1_e32 v145, v146
	v_cvt_f32_ubyte0_e32 v144, v146
	v_cvt_f32_ubyte1_e32 v163, v147
	v_cvt_f32_ubyte0_e32 v162, v147
	v_cvt_f32_ubyte3_e32 v173, v146
	v_cvt_f32_ubyte2_e32 v172, v146
	v_cvt_f32_ubyte3_e32 v179, v147
	v_cvt_f32_ubyte2_e32 v178, v147
	v_pk_mul_f32 v[144:145], v[144:145], s[28:29] op_sel_hi:[1,0]
	v_pk_mul_f32 v[162:163], v[162:163], s[28:29] op_sel_hi:[1,0]
	v_pk_mul_f32 v[172:173], v[172:173], s[28:29] op_sel_hi:[1,0]
	v_pk_mul_f32 v[146:147], v[178:179], s[28:29] op_sel_hi:[1,0]
	v_pk_mul_f32 v[144:145], v[84:85], v[144:145]
	v_pk_mul_f32 v[162:163], v[80:81], v[162:163]
	v_pk_mul_f32 v[172:173], v[86:87], v[172:173]
	v_pk_mul_f32 v[178:179], v[82:83], v[146:147]
	v_cvt_pk_bf16_f32 v144, v144, v145
	v_cvt_pk_bf16_f32 v145, v172, v173
	v_cvt_pk_bf16_f32 v146, v162, v163
	v_cvt_pk_bf16_f32 v147, v178, v179
	global_store_dwordx4 v[160:161], v[144:147], off offset:256
	v_cvt_f32_ubyte3_e32 v161, v140
	v_cvt_f32_ubyte2_e32 v160, v140
	v_cvt_f32_ubyte1_e32 v145, v140
	v_cvt_f32_ubyte0_e32 v144, v140
	v_cvt_f32_ubyte1_e32 v147, v141
	v_cvt_f32_ubyte0_e32 v146, v141
	v_cvt_f32_ubyte3_e32 v163, v141
	v_cvt_f32_ubyte2_e32 v162, v141
	v_pk_mul_f32 v[144:145], v[144:145], s[28:29] op_sel_hi:[1,0]
	v_pk_mul_f32 v[146:147], v[146:147], s[28:29] op_sel_hi:[1,0]
	v_pk_mul_f32 v[160:161], v[160:161], s[28:29] op_sel_hi:[1,0]
	v_pk_mul_f32 v[140:141], v[162:163], s[28:29] op_sel_hi:[1,0]
	v_pk_mul_f32 v[144:145], v[76:77], v[144:145]
	v_pk_mul_f32 v[146:147], v[72:73], v[146:147]
	v_pk_mul_f32 v[160:161], v[78:79], v[160:161]
	v_pk_mul_f32 v[140:141], v[74:75], v[140:141]
	v_cvt_pk_bf16_f32 v144, v144, v145
	v_cvt_pk_bf16_f32 v145, v160, v161
	v_cvt_pk_bf16_f32 v146, v146, v147
	v_cvt_pk_bf16_f32 v147, v140, v141
	global_store_dwordx4 v[156:157], v[144:147], off offset:256
	v_cvt_f32_ubyte1_e32 v141, v142
	v_cvt_f32_ubyte0_e32 v140, v142
	v_cvt_f32_ubyte1_e32 v145, v143
	v_cvt_f32_ubyte0_e32 v144, v143
	v_cvt_f32_ubyte3_e32 v147, v142
	v_cvt_f32_ubyte2_e32 v146, v142
	v_cvt_f32_ubyte3_e32 v157, v143
	v_cvt_f32_ubyte2_e32 v156, v143
	v_pk_mul_f32 v[140:141], v[140:141], s[28:29] op_sel_hi:[1,0]
	v_pk_mul_f32 v[144:145], v[144:145], s[28:29] op_sel_hi:[1,0]
	v_pk_mul_f32 v[146:147], v[146:147], s[28:29] op_sel_hi:[1,0]
	v_pk_mul_f32 v[142:143], v[156:157], s[28:29] op_sel_hi:[1,0]
	v_pk_mul_f32 v[140:141], v[68:69], v[140:141]
	v_pk_mul_f32 v[144:145], v[64:65], v[144:145]
	v_pk_mul_f32 v[146:147], v[70:71], v[146:147]
	v_pk_mul_f32 v[156:157], v[66:67], v[142:143]
	v_cvt_pk_bf16_f32 v140, v140, v141
	v_cvt_pk_bf16_f32 v141, v146, v147
	v_cvt_pk_bf16_f32 v142, v144, v145
	v_cvt_pk_bf16_f32 v143, v156, v157
	global_store_dwordx4 v[158:159], v[140:143], off offset:256
	v_cvt_f32_ubyte3_e32 v145, v136
	v_cvt_f32_ubyte2_e32 v144, v136
	v_cvt_f32_ubyte1_e32 v141, v136
	v_cvt_f32_ubyte0_e32 v140, v136
	v_cvt_f32_ubyte1_e32 v143, v137
	v_cvt_f32_ubyte0_e32 v142, v137
	v_cvt_f32_ubyte3_e32 v147, v137
	v_cvt_f32_ubyte2_e32 v146, v137
	v_pk_mul_f32 v[140:141], v[140:141], s[28:29] op_sel_hi:[1,0]
	v_pk_mul_f32 v[142:143], v[142:143], s[28:29] op_sel_hi:[1,0]
	v_pk_mul_f32 v[144:145], v[144:145], s[28:29] op_sel_hi:[1,0]
	v_pk_mul_f32 v[136:137], v[146:147], s[28:29] op_sel_hi:[1,0]
	v_pk_mul_f32 v[140:141], v[28:29], v[140:141]
	v_pk_mul_f32 v[142:143], v[24:25], v[142:143]
	v_pk_mul_f32 v[144:145], v[30:31], v[144:145]
	v_pk_mul_f32 v[136:137], v[26:27], v[136:137]
	v_cvt_pk_bf16_f32 v140, v140, v141
	v_cvt_pk_bf16_f32 v141, v144, v145
	v_cvt_pk_bf16_f32 v142, v142, v143
	v_cvt_pk_bf16_f32 v143, v136, v137
	global_store_dwordx4 v[152:153], v[140:143], off offset:256
	v_cvt_f32_ubyte1_e32 v137, v138
	v_cvt_f32_ubyte0_e32 v136, v138
	v_cvt_f32_ubyte1_e32 v141, v139
	v_cvt_f32_ubyte0_e32 v140, v139
	v_cvt_f32_ubyte3_e32 v143, v138
	v_cvt_f32_ubyte2_e32 v142, v138
	v_cvt_f32_ubyte3_e32 v145, v139
	v_cvt_f32_ubyte2_e32 v144, v139
	v_pk_mul_f32 v[136:137], v[136:137], s[28:29] op_sel_hi:[1,0]
	v_pk_mul_f32 v[140:141], v[140:141], s[28:29] op_sel_hi:[1,0]
	v_pk_mul_f32 v[142:143], v[142:143], s[28:29] op_sel_hi:[1,0]
	v_pk_mul_f32 v[138:139], v[144:145], s[28:29] op_sel_hi:[1,0]
	v_pk_mul_f32 v[136:137], v[20:21], v[136:137]
	v_pk_mul_f32 v[140:141], v[16:17], v[140:141]
	v_pk_mul_f32 v[142:143], v[22:23], v[142:143]
	v_pk_mul_f32 v[144:145], v[18:19], v[138:139]
	v_cvt_pk_bf16_f32 v136, v136, v137
	v_cvt_pk_bf16_f32 v137, v142, v143
	v_cvt_pk_bf16_f32 v138, v140, v141
	v_cvt_pk_bf16_f32 v139, v144, v145
	global_store_dwordx4 v[154:155], v[136:139], off offset:256
	v_cvt_f32_ubyte3_e32 v141, v132
	v_cvt_f32_ubyte2_e32 v140, v132
	v_cvt_f32_ubyte1_e32 v137, v132
	v_cvt_f32_ubyte0_e32 v136, v132
	v_cvt_f32_ubyte1_e32 v139, v133
	v_cvt_f32_ubyte0_e32 v138, v133
	v_cvt_f32_ubyte3_e32 v143, v133
	v_cvt_f32_ubyte2_e32 v142, v133
	v_pk_mul_f32 v[136:137], v[136:137], s[28:29] op_sel_hi:[1,0]
	v_pk_mul_f32 v[138:139], v[138:139], s[28:29] op_sel_hi:[1,0]
	v_pk_mul_f32 v[140:141], v[140:141], s[28:29] op_sel_hi:[1,0]
	v_pk_mul_f32 v[132:133], v[142:143], s[28:29] op_sel_hi:[1,0]
	v_pk_mul_f32 v[136:137], v[12:13], v[136:137]
	v_pk_mul_f32 v[138:139], v[8:9], v[138:139]
	v_pk_mul_f32 v[140:141], v[14:15], v[140:141]
	v_pk_mul_f32 v[132:133], v[10:11], v[132:133]
	v_cvt_pk_bf16_f32 v136, v136, v137
	v_cvt_pk_bf16_f32 v137, v140, v141
	v_cvt_pk_bf16_f32 v138, v138, v139
	v_cvt_pk_bf16_f32 v139, v132, v133
	global_store_dwordx4 v[148:149], v[136:139], off offset:256
	v_cvt_f32_ubyte1_e32 v133, v134
	v_cvt_f32_ubyte0_e32 v132, v134
	v_cvt_f32_ubyte1_e32 v137, v135
	v_cvt_f32_ubyte0_e32 v136, v135
	v_cvt_f32_ubyte3_e32 v139, v134
	v_cvt_f32_ubyte2_e32 v138, v134
	v_cvt_f32_ubyte3_e32 v141, v135
	v_cvt_f32_ubyte2_e32 v140, v135
	v_pk_mul_f32 v[132:133], v[132:133], s[28:29] op_sel_hi:[1,0]
	v_pk_mul_f32 v[136:137], v[136:137], s[28:29] op_sel_hi:[1,0]
	v_pk_mul_f32 v[138:139], v[138:139], s[28:29] op_sel_hi:[1,0]
	v_pk_mul_f32 v[134:135], v[140:141], s[28:29] op_sel_hi:[1,0]
	v_pk_mul_f32 v[132:133], v[4:5], v[132:133]
	v_pk_mul_f32 v[136:137], v[0:1], v[136:137]
	v_pk_mul_f32 v[138:139], v[6:7], v[138:139]
	v_pk_mul_f32 v[140:141], v[2:3], v[134:135]
	v_cvt_pk_bf16_f32 v132, v132, v133
	v_cvt_pk_bf16_f32 v133, v138, v139
	v_cvt_pk_bf16_f32 v134, v136, v137
	v_cvt_pk_bf16_f32 v135, v140, v141
	global_store_dwordx4 v[150:151], v[132:135], off offset:256
	s_mov_b32 s37, s8
	s_mov_b32 s75, s88
	s_cbranch_execnz .LBB0_763
.LBB0_765:
	v_add_co_u32_e32 v132, vcc, 0x8800000, v114
	global_load_dwordx4 v[156:159], v[114:115], off nt
	s_nop 0
	v_addc_co_u32_e32 v133, vcc, 0, v115, vcc
	global_load_dwordx4 v[160:163], v[132:133], off nt
	v_add_co_u32_e32 v132, vcc, 0x2000, v114
	s_mov_b32 s7, 0x8808000
	s_nop 0
	v_addc_co_u32_e32 v133, vcc, 0, v115, vcc
	global_load_dwordx4 v[148:151], v[132:133], off nt
	v_add_co_u32_e32 v132, vcc, 0x8802000, v114
	s_waitcnt vmcnt(0)
	v_cvt_f32_ubyte1_e32 v187, v156
	v_addc_co_u32_e32 v133, vcc, 0, v115, vcc
	global_load_dwordx4 v[152:155], v[132:133], off nt
	v_add_co_u32_e32 v132, vcc, 0x4000, v114
	v_cvt_f32_ubyte0_e32 v112, v160
	s_nop 0
	v_addc_co_u32_e32 v133, vcc, 0, v115, vcc
	global_load_dwordx4 v[140:143], v[132:133], off nt
	v_add_co_u32_e32 v132, vcc, 0x8804000, v114
	v_rcp_iflag_f32_e32 v172, v112
	s_nop 0
	v_addc_co_u32_e32 v133, vcc, 0, v115, vcc
	global_load_dwordx4 v[144:147], v[132:133], off nt
	v_add_co_u32_e32 v132, vcc, s89, v114
	v_cvt_f32_ubyte0_e32 v112, v161
	s_nop 0
	v_addc_co_u32_e32 v133, vcc, 0, v115, vcc
	v_add_co_u32_e32 v136, vcc, 0x8806000, v114
	global_load_dwordx4 v[132:135], v[132:133], off nt
	s_nop 0
	v_addc_co_u32_e32 v137, vcc, 0, v115, vcc
	global_load_dwordx4 v[136:139], v[136:137], off nt
	v_rcp_iflag_f32_e32 v178, v112
	v_cvt_f32_ubyte1_e32 v112, v160
	v_rcp_iflag_f32_e32 v173, v112
	v_cvt_f32_ubyte1_e32 v112, v161
	v_rcp_iflag_f32_e32 v179, v112
	v_cvt_f32_ubyte2_e32 v112, v160
	v_rcp_iflag_f32_e32 v180, v112
	v_cvt_f32_ubyte2_e32 v112, v161
	v_rcp_iflag_f32_e32 v182, v112
	v_cvt_f32_ubyte3_e32 v112, v160
	v_rcp_iflag_f32_e32 v181, v112
	v_cvt_f32_ubyte3_e32 v112, v161
	v_cvt_f32_ubyte0_e32 v186, v156
	v_rcp_iflag_f32_e32 v183, v112
	v_pk_mul_f32 v[172:173], v[172:173], v[186:187]
	v_cvt_f32_ubyte3_e32 v185, v156
	v_pk_mul_f32 v[128:129], v[128:129], v[172:173]
	v_cvt_f32_ubyte1_e32 v173, v157
	v_cvt_f32_ubyte0_e32 v172, v157
	v_cvt_f32_ubyte2_e32 v184, v156
	v_cvt_f32_ubyte3_e32 v161, v157
	v_cvt_f32_ubyte2_e32 v160, v157
	v_pk_mul_f32 v[156:157], v[178:179], v[172:173]
	v_cvt_f32_ubyte0_e32 v112, v162
	v_pk_mul_f32 v[160:161], v[182:183], v[160:161]
	v_pk_mul_f32 v[124:125], v[124:125], v[156:157]
	v_rcp_iflag_f32_e32 v156, v112
	v_cvt_f32_ubyte0_e32 v112, v163
	v_pk_mul_f32 v[126:127], v[126:127], v[160:161]
	v_rcp_iflag_f32_e32 v160, v112
	v_cvt_f32_ubyte1_e32 v112, v162
	v_rcp_iflag_f32_e32 v157, v112
	v_cvt_f32_ubyte1_e32 v112, v163
	v_rcp_iflag_f32_e32 v161, v112
	v_cvt_f32_ubyte2_e32 v112, v162
	v_rcp_iflag_f32_e32 v172, v112
	v_cvt_f32_ubyte2_e32 v112, v163
	v_rcp_iflag_f32_e32 v178, v112
	v_cvt_f32_ubyte3_e32 v112, v162
	v_rcp_iflag_f32_e32 v173, v112
	v_cvt_f32_ubyte3_e32 v112, v163
	v_rcp_iflag_f32_e32 v179, v112
	v_cvt_f32_ubyte1_e32 v183, v158
	v_cvt_f32_ubyte0_e32 v182, v158
	v_pk_mul_f32 v[156:157], v[156:157], v[182:183]
	v_pk_mul_f32 v[180:181], v[180:181], v[184:185]
	v_pk_mul_f32 v[120:121], v[120:121], v[156:157]
	v_cvt_f32_ubyte3_e32 v157, v159
	v_cvt_f32_ubyte2_e32 v156, v159
	v_cvt_f32_ubyte1_e32 v163, v159
	v_cvt_f32_ubyte0_e32 v162, v159
	v_pk_mul_f32 v[156:157], v[178:179], v[156:157]
	v_pk_mul_f32 v[130:131], v[130:131], v[180:181]
	v_cvt_f32_ubyte3_e32 v181, v158
	v_cvt_f32_ubyte2_e32 v180, v158
	v_pk_mul_f32 v[158:159], v[160:161], v[162:163]
	s_waitcnt vmcnt(4)
	v_cvt_f32_ubyte0_e32 v112, v152
	v_pk_mul_f32 v[118:119], v[118:119], v[156:157]
	v_rcp_iflag_f32_e32 v156, v112
	v_cvt_f32_ubyte0_e32 v112, v153
	v_pk_mul_f32 v[116:117], v[116:117], v[158:159]
	v_rcp_iflag_f32_e32 v158, v112
	v_cvt_f32_ubyte1_e32 v112, v152
	v_rcp_iflag_f32_e32 v157, v112
	v_cvt_f32_ubyte1_e32 v112, v153
	v_rcp_iflag_f32_e32 v159, v112
	v_cvt_f32_ubyte2_e32 v112, v152
	v_rcp_iflag_f32_e32 v160, v112
	v_cvt_f32_ubyte2_e32 v112, v153
	v_rcp_iflag_f32_e32 v162, v112
	v_cvt_f32_ubyte3_e32 v112, v152
	v_rcp_iflag_f32_e32 v161, v112
	v_cvt_f32_ubyte3_e32 v112, v153
	v_cvt_f32_ubyte1_e32 v179, v148
	v_cvt_f32_ubyte0_e32 v178, v148
	v_rcp_iflag_f32_e32 v163, v112
	v_pk_mul_f32 v[156:157], v[156:157], v[178:179]
	v_pk_mul_f32 v[172:173], v[172:173], v[180:181]
	v_pk_mul_f32 v[108:109], v[108:109], v[156:157]
	v_cvt_f32_ubyte1_e32 v157, v149
	v_cvt_f32_ubyte0_e32 v156, v149
	v_pk_mul_f32 v[122:123], v[122:123], v[172:173]
	v_cvt_f32_ubyte3_e32 v173, v148
	v_cvt_f32_ubyte2_e32 v172, v148
	v_cvt_f32_ubyte3_e32 v153, v149
	v_cvt_f32_ubyte2_e32 v152, v149
	v_pk_mul_f32 v[148:149], v[158:159], v[156:157]
	v_cvt_f32_ubyte0_e32 v112, v154
	v_pk_mul_f32 v[152:153], v[162:163], v[152:153]
	v_pk_mul_f32 v[104:105], v[104:105], v[148:149]
	v_rcp_iflag_f32_e32 v148, v112
	v_cvt_f32_ubyte0_e32 v112, v155
	v_pk_mul_f32 v[106:107], v[106:107], v[152:153]
	v_rcp_iflag_f32_e32 v152, v112
	v_cvt_f32_ubyte1_e32 v112, v154
	v_rcp_iflag_f32_e32 v149, v112
	v_cvt_f32_ubyte1_e32 v112, v155
	v_rcp_iflag_f32_e32 v153, v112
	v_cvt_f32_ubyte2_e32 v112, v154
	v_rcp_iflag_f32_e32 v156, v112
	v_cvt_f32_ubyte2_e32 v112, v155
	v_rcp_iflag_f32_e32 v158, v112
	v_cvt_f32_ubyte3_e32 v112, v154
	v_rcp_iflag_f32_e32 v157, v112
	v_cvt_f32_ubyte3_e32 v112, v155
	v_rcp_iflag_f32_e32 v159, v112
	v_cvt_f32_ubyte1_e32 v163, v150
	v_cvt_f32_ubyte0_e32 v162, v150
	v_pk_mul_f32 v[148:149], v[148:149], v[162:163]
	v_pk_mul_f32 v[160:161], v[160:161], v[172:173]
	v_pk_mul_f32 v[100:101], v[100:101], v[148:149]
	v_cvt_f32_ubyte3_e32 v149, v151
	v_cvt_f32_ubyte2_e32 v148, v151
	v_pk_mul_f32 v[148:149], v[158:159], v[148:149]
	v_pk_mul_f32 v[110:111], v[110:111], v[160:161]
	v_cvt_f32_ubyte3_e32 v161, v150
	v_cvt_f32_ubyte2_e32 v160, v150
	v_pk_mul_f32 v[98:99], v[98:99], v[148:149]
	v_add_co_u32_e32 v148, vcc, s24, v114
	v_pk_mul_f32 v[156:157], v[156:157], v[160:161]
	s_nop 0
	v_addc_co_u32_e32 v149, vcc, 0, v115, vcc
	s_waitcnt vmcnt(2)
	v_cvt_f32_ubyte0_e32 v112, v144
	v_pk_mul_f32 v[102:103], v[102:103], v[156:157]
	global_load_dwordx4 v[156:159], v[148:149], off nt
	v_add_co_u32_e32 v148, vcc, s7, v114
	v_rcp_iflag_f32_e32 v172, v112
	v_cvt_f32_ubyte0_e32 v112, v145
	v_addc_co_u32_e32 v149, vcc, 0, v115, vcc
	v_rcp_iflag_f32_e32 v178, v112
	v_cvt_f32_ubyte1_e32 v112, v144
	global_load_dwordx4 v[160:163], v[148:149], off nt
	v_rcp_iflag_f32_e32 v173, v112
	v_cvt_f32_ubyte1_e32 v112, v145
	v_rcp_iflag_f32_e32 v179, v112
	v_cvt_f32_ubyte2_e32 v112, v144
	v_rcp_iflag_f32_e32 v180, v112
	v_cvt_f32_ubyte2_e32 v112, v145
	v_rcp_iflag_f32_e32 v182, v112
	v_cvt_f32_ubyte3_e32 v112, v144
	v_rcp_iflag_f32_e32 v181, v112
	v_cvt_f32_ubyte3_e32 v112, v145
	v_cvt_f32_ubyte1_e32 v187, v140
	v_cvt_f32_ubyte0_e32 v186, v140
	v_rcp_iflag_f32_e32 v183, v112
	v_pk_mul_f32 v[172:173], v[172:173], v[186:187]
	v_cvt_f32_ubyte3_e32 v185, v140
	v_pk_mul_f32 v[60:61], v[60:61], v[172:173]
	v_cvt_f32_ubyte1_e32 v173, v141
	v_cvt_f32_ubyte0_e32 v172, v141
	v_cvt_f32_ubyte2_e32 v184, v140
	v_cvt_f32_ubyte3_e32 v145, v141
	v_cvt_f32_ubyte2_e32 v144, v141
	v_pk_mul_f32 v[140:141], v[178:179], v[172:173]
	v_cvt_f32_ubyte0_e32 v112, v146
	v_pk_mul_f32 v[144:145], v[182:183], v[144:145]
	v_pk_mul_f32 v[56:57], v[56:57], v[140:141]
	v_rcp_iflag_f32_e32 v140, v112
	v_cvt_f32_ubyte0_e32 v112, v147
	v_pk_mul_f32 v[58:59], v[58:59], v[144:145]
	v_rcp_iflag_f32_e32 v144, v112
	v_cvt_f32_ubyte1_e32 v112, v146
	v_rcp_iflag_f32_e32 v141, v112
	v_cvt_f32_ubyte1_e32 v112, v147
	v_rcp_iflag_f32_e32 v145, v112
	v_cvt_f32_ubyte2_e32 v112, v146
	v_rcp_iflag_f32_e32 v172, v112
	v_cvt_f32_ubyte2_e32 v112, v147
	v_rcp_iflag_f32_e32 v178, v112
	v_cvt_f32_ubyte3_e32 v112, v146
	v_rcp_iflag_f32_e32 v173, v112
	v_cvt_f32_ubyte3_e32 v112, v147
	v_rcp_iflag_f32_e32 v179, v112
	v_cvt_f32_ubyte1_e32 v183, v142
	v_cvt_f32_ubyte0_e32 v182, v142
	v_pk_mul_f32 v[140:141], v[140:141], v[182:183]
	s_mov_b32 s7, 0xa000
	v_pk_mul_f32 v[52:53], v[52:53], v[140:141]
	v_cvt_f32_ubyte3_e32 v141, v143
	v_cvt_f32_ubyte2_e32 v140, v143
	v_add_co_u32_e32 v148, vcc, s7, v114
	v_pk_mul_f32 v[180:181], v[180:181], v[184:185]
	v_cvt_f32_ubyte1_e32 v147, v143
	v_cvt_f32_ubyte0_e32 v146, v143
	v_pk_mul_f32 v[140:141], v[178:179], v[140:141]
	s_waitcnt vmcnt(2)
	v_cvt_f32_ubyte0_e32 v112, v136
	v_cvt_f32_ubyte1_e32 v155, v151
	v_cvt_f32_ubyte0_e32 v154, v151
	v_addc_co_u32_e32 v149, vcc, 0, v115, vcc
	s_mov_b32 s7, 0x880a000
	v_pk_mul_f32 v[62:63], v[62:63], v[180:181]
	v_cvt_f32_ubyte3_e32 v181, v142
	v_cvt_f32_ubyte2_e32 v180, v142
	v_pk_mul_f32 v[142:143], v[144:145], v[146:147]
	v_pk_mul_f32 v[50:51], v[50:51], v[140:141]
	v_rcp_iflag_f32_e32 v140, v112
	v_cvt_f32_ubyte0_e32 v112, v137
	v_pk_mul_f32 v[150:151], v[152:153], v[154:155]
	v_add_co_u32_e32 v152, vcc, s7, v114
	v_pk_mul_f32 v[48:49], v[48:49], v[142:143]
	v_rcp_iflag_f32_e32 v142, v112
	v_cvt_f32_ubyte1_e32 v112, v136
	v_addc_co_u32_e32 v153, vcc, 0, v115, vcc
	v_rcp_iflag_f32_e32 v141, v112
	v_cvt_f32_ubyte1_e32 v112, v137
	global_load_dwordx4 v[152:155], v[152:153], off nt
	v_rcp_iflag_f32_e32 v143, v112
	v_cvt_f32_ubyte2_e32 v112, v136
	v_rcp_iflag_f32_e32 v144, v112
	v_cvt_f32_ubyte2_e32 v112, v137
	v_rcp_iflag_f32_e32 v146, v112
	v_cvt_f32_ubyte3_e32 v112, v136
	v_rcp_iflag_f32_e32 v145, v112
	v_cvt_f32_ubyte3_e32 v112, v137
	v_cvt_f32_ubyte1_e32 v179, v132
	v_cvt_f32_ubyte0_e32 v178, v132
	v_rcp_iflag_f32_e32 v147, v112
	v_pk_mul_f32 v[140:141], v[140:141], v[178:179]
	v_pk_mul_f32 v[172:173], v[172:173], v[180:181]
	v_pk_mul_f32 v[44:45], v[44:45], v[140:141]
	v_cvt_f32_ubyte1_e32 v141, v133
	v_cvt_f32_ubyte0_e32 v140, v133
	v_pk_mul_f32 v[54:55], v[54:55], v[172:173]
	v_cvt_f32_ubyte3_e32 v173, v132
	v_cvt_f32_ubyte2_e32 v172, v132
	v_cvt_f32_ubyte3_e32 v137, v133
	v_cvt_f32_ubyte2_e32 v136, v133
	v_pk_mul_f32 v[132:133], v[142:143], v[140:141]
	v_cvt_f32_ubyte0_e32 v112, v138
	v_pk_mul_f32 v[136:137], v[146:147], v[136:137]
	v_pk_mul_f32 v[40:41], v[40:41], v[132:133]
	v_rcp_iflag_f32_e32 v132, v112
	v_cvt_f32_ubyte0_e32 v112, v139
	v_pk_mul_f32 v[96:97], v[96:97], v[150:151]
	global_load_dwordx4 v[148:151], v[148:149], off nt
	v_pk_mul_f32 v[42:43], v[42:43], v[136:137]
	v_rcp_iflag_f32_e32 v136, v112
	v_cvt_f32_ubyte1_e32 v112, v138
	v_rcp_iflag_f32_e32 v133, v112
	v_cvt_f32_ubyte1_e32 v112, v139
	v_rcp_iflag_f32_e32 v137, v112
	v_cvt_f32_ubyte2_e32 v112, v138
	v_rcp_iflag_f32_e32 v140, v112
	v_cvt_f32_ubyte2_e32 v112, v139
	v_rcp_iflag_f32_e32 v142, v112
	v_cvt_f32_ubyte3_e32 v112, v138
	v_rcp_iflag_f32_e32 v141, v112
	v_cvt_f32_ubyte3_e32 v112, v139
	v_rcp_iflag_f32_e32 v143, v112
	v_cvt_f32_ubyte1_e32 v147, v134
	v_cvt_f32_ubyte0_e32 v146, v134
	v_pk_mul_f32 v[132:133], v[132:133], v[146:147]
	v_pk_mul_f32 v[144:145], v[144:145], v[172:173]
	v_pk_mul_f32 v[36:37], v[36:37], v[132:133]
	v_cvt_f32_ubyte3_e32 v133, v135
	v_cvt_f32_ubyte2_e32 v132, v135
	v_pk_mul_f32 v[132:133], v[142:143], v[132:133]
	s_mov_b32 s7, 0xc000
	v_pk_mul_f32 v[46:47], v[46:47], v[144:145]
	v_cvt_f32_ubyte3_e32 v145, v134
	v_cvt_f32_ubyte2_e32 v144, v134
	v_pk_mul_f32 v[34:35], v[34:35], v[132:133]
	v_add_co_u32_e32 v132, vcc, s7, v114
	v_pk_mul_f32 v[140:141], v[140:141], v[144:145]
	s_nop 0
	v_addc_co_u32_e32 v133, vcc, 0, v115, vcc
	s_mov_b32 s7, 0x880c000
	v_pk_mul_f32 v[38:39], v[38:39], v[140:141]
	global_load_dwordx4 v[140:143], v[132:133], off nt
	v_add_co_u32_e32 v132, vcc, s7, v114
	s_mov_b32 s7, 0xe000
	s_nop 0
	v_addc_co_u32_e32 v133, vcc, 0, v115, vcc
	global_load_dwordx4 v[144:147], v[132:133], off nt
	v_add_co_u32_e32 v132, vcc, s7, v114
	s_mov_b32 s7, 0x880e000
	s_nop 0
	v_addc_co_u32_e32 v133, vcc, 0, v115, vcc
	v_cvt_f32_ubyte1_e32 v139, v135
	v_cvt_f32_ubyte0_e32 v138, v135
	v_add_co_u32_e32 v114, vcc, s7, v114
	v_pk_mul_f32 v[134:135], v[136:137], v[138:139]
	s_nop 0
	v_addc_co_u32_e32 v115, vcc, 0, v115, vcc
	v_pk_mul_f32 v[32:33], v[32:33], v[134:135]
	global_load_dwordx4 v[132:135], v[132:133], off nt
	s_waitcnt vmcnt(5)
	v_cvt_f32_ubyte0_e32 v112, v160
	global_load_dwordx4 v[136:139], v[114:115], off nt
	v_rcp_iflag_f32_e32 v114, v112
	v_cvt_f32_ubyte0_e32 v112, v161
	v_rcp_iflag_f32_e32 v172, v112
	v_cvt_f32_ubyte1_e32 v112, v160
	v_rcp_iflag_f32_e32 v115, v112
	v_cvt_f32_ubyte1_e32 v112, v161
	v_rcp_iflag_f32_e32 v173, v112
	v_cvt_f32_ubyte2_e32 v112, v160
	v_rcp_iflag_f32_e32 v178, v112
	v_cvt_f32_ubyte2_e32 v112, v161
	v_rcp_iflag_f32_e32 v180, v112
	v_cvt_f32_ubyte3_e32 v112, v160
	v_rcp_iflag_f32_e32 v179, v112
	v_cvt_f32_ubyte3_e32 v112, v161
	v_rcp_iflag_f32_e32 v181, v112
	v_cvt_f32_ubyte1_e32 v185, v156
	v_cvt_f32_ubyte0_e32 v184, v156
	v_pk_mul_f32 v[114:115], v[114:115], v[184:185]
	v_cvt_f32_ubyte1_e32 v161, v157
	v_pk_mul_f32 v[92:93], v[92:93], v[114:115]
	v_cvt_f32_ubyte3_e32 v115, v157
	v_cvt_f32_ubyte2_e32 v114, v157
	v_cvt_f32_ubyte0_e32 v160, v157
	v_pk_mul_f32 v[114:115], v[180:181], v[114:115]
	v_cvt_f32_ubyte0_e32 v112, v162
	v_cvt_f32_ubyte3_e32 v183, v156
	v_cvt_f32_ubyte2_e32 v182, v156
	v_pk_mul_f32 v[156:157], v[172:173], v[160:161]
	v_pk_mul_f32 v[90:91], v[90:91], v[114:115]
	v_rcp_iflag_f32_e32 v114, v112
	v_cvt_f32_ubyte0_e32 v112, v163
	v_pk_mul_f32 v[88:89], v[88:89], v[156:157]
	v_rcp_iflag_f32_e32 v156, v112
	v_cvt_f32_ubyte1_e32 v112, v162
	v_rcp_iflag_f32_e32 v115, v112
	v_cvt_f32_ubyte1_e32 v112, v163
	v_rcp_iflag_f32_e32 v157, v112
	v_cvt_f32_ubyte2_e32 v112, v162
	v_rcp_iflag_f32_e32 v160, v112
	v_cvt_f32_ubyte2_e32 v112, v163
	v_rcp_iflag_f32_e32 v172, v112
	v_cvt_f32_ubyte3_e32 v112, v162
	v_rcp_iflag_f32_e32 v161, v112
	v_cvt_f32_ubyte3_e32 v112, v163
	v_rcp_iflag_f32_e32 v173, v112
	v_pk_mul_f32 v[178:179], v[178:179], v[182:183]
	v_cvt_f32_ubyte1_e32 v181, v158
	v_cvt_f32_ubyte0_e32 v180, v158
	v_pk_mul_f32 v[94:95], v[94:95], v[178:179]
	v_cvt_f32_ubyte3_e32 v179, v158
	v_cvt_f32_ubyte2_e32 v178, v158
	v_pk_mul_f32 v[114:115], v[114:115], v[180:181]
	v_pk_mul_f32 v[160:161], v[160:161], v[178:179]
	v_pk_mul_f32 v[84:85], v[84:85], v[114:115]
	v_cvt_f32_ubyte3_e32 v115, v159
	v_cvt_f32_ubyte2_e32 v114, v159
	v_pk_mul_f32 v[86:87], v[86:87], v[160:161]
	v_cvt_f32_ubyte1_e32 v161, v159
	v_cvt_f32_ubyte0_e32 v160, v159
	v_pk_mul_f32 v[114:115], v[172:173], v[114:115]
	s_waitcnt vmcnt(5)
	v_cvt_f32_ubyte0_e32 v112, v152
	v_pk_mul_f32 v[156:157], v[156:157], v[160:161]
	v_pk_mul_f32 v[82:83], v[82:83], v[114:115]
	v_rcp_iflag_f32_e32 v114, v112
	v_cvt_f32_ubyte0_e32 v112, v153
	v_pk_mul_f32 v[80:81], v[80:81], v[156:157]
	v_rcp_iflag_f32_e32 v156, v112
	v_cvt_f32_ubyte1_e32 v112, v152
	v_rcp_iflag_f32_e32 v115, v112
	v_cvt_f32_ubyte1_e32 v112, v153
	v_rcp_iflag_f32_e32 v157, v112
	v_cvt_f32_ubyte2_e32 v112, v152
	v_rcp_iflag_f32_e32 v158, v112
	v_cvt_f32_ubyte2_e32 v112, v153
	v_rcp_iflag_f32_e32 v160, v112
	v_cvt_f32_ubyte3_e32 v112, v152
	v_rcp_iflag_f32_e32 v159, v112
	v_cvt_f32_ubyte3_e32 v112, v153
	v_rcp_iflag_f32_e32 v161, v112
	s_waitcnt vmcnt(4)
	v_cvt_f32_ubyte1_e32 v173, v148
	v_cvt_f32_ubyte0_e32 v172, v148
	v_pk_mul_f32 v[114:115], v[114:115], v[172:173]
	v_cvt_f32_ubyte1_e32 v153, v149
	v_pk_mul_f32 v[76:77], v[76:77], v[114:115]
	v_cvt_f32_ubyte3_e32 v115, v149
	v_cvt_f32_ubyte2_e32 v114, v149
	v_cvt_f32_ubyte0_e32 v152, v149
	v_pk_mul_f32 v[114:115], v[160:161], v[114:115]
	v_cvt_f32_ubyte0_e32 v112, v154
	v_cvt_f32_ubyte3_e32 v163, v148
	v_cvt_f32_ubyte2_e32 v162, v148
	v_pk_mul_f32 v[148:149], v[156:157], v[152:153]
	v_pk_mul_f32 v[74:75], v[74:75], v[114:115]
	v_rcp_iflag_f32_e32 v114, v112
	v_cvt_f32_ubyte0_e32 v112, v155
	v_pk_mul_f32 v[72:73], v[72:73], v[148:149]
	v_rcp_iflag_f32_e32 v148, v112
	v_cvt_f32_ubyte1_e32 v112, v154
	v_rcp_iflag_f32_e32 v115, v112
	v_cvt_f32_ubyte1_e32 v112, v155
	v_rcp_iflag_f32_e32 v149, v112
	v_cvt_f32_ubyte2_e32 v112, v154
	v_rcp_iflag_f32_e32 v152, v112
	v_cvt_f32_ubyte2_e32 v112, v155
	v_rcp_iflag_f32_e32 v156, v112
	v_cvt_f32_ubyte3_e32 v112, v154
	v_rcp_iflag_f32_e32 v153, v112
	v_cvt_f32_ubyte3_e32 v112, v155
	v_rcp_iflag_f32_e32 v157, v112
	v_pk_mul_f32 v[158:159], v[158:159], v[162:163]
	v_cvt_f32_ubyte1_e32 v161, v150
	v_cvt_f32_ubyte0_e32 v160, v150
	v_pk_mul_f32 v[78:79], v[78:79], v[158:159]
	v_cvt_f32_ubyte3_e32 v159, v150
	v_cvt_f32_ubyte2_e32 v158, v150
	v_pk_mul_f32 v[114:115], v[114:115], v[160:161]
	v_pk_mul_f32 v[152:153], v[152:153], v[158:159]
	v_pk_mul_f32 v[68:69], v[68:69], v[114:115]
	v_cvt_f32_ubyte3_e32 v115, v151
	v_cvt_f32_ubyte2_e32 v114, v151
	v_pk_mul_f32 v[70:71], v[70:71], v[152:153]
	v_cvt_f32_ubyte1_e32 v153, v151
	v_cvt_f32_ubyte0_e32 v152, v151
	v_pk_mul_f32 v[114:115], v[156:157], v[114:115]
	s_waitcnt vmcnt(2)
	v_cvt_f32_ubyte0_e32 v112, v144
	v_pk_mul_f32 v[148:149], v[148:149], v[152:153]
	v_pk_mul_f32 v[66:67], v[66:67], v[114:115]
	v_rcp_iflag_f32_e32 v114, v112
	v_cvt_f32_ubyte0_e32 v112, v145
	v_pk_mul_f32 v[64:65], v[64:65], v[148:149]
	v_rcp_iflag_f32_e32 v148, v112
	v_cvt_f32_ubyte1_e32 v112, v144
	v_rcp_iflag_f32_e32 v115, v112
	v_cvt_f32_ubyte1_e32 v112, v145
	v_rcp_iflag_f32_e32 v149, v112
	v_cvt_f32_ubyte2_e32 v112, v144
	v_rcp_iflag_f32_e32 v150, v112
	v_cvt_f32_ubyte2_e32 v112, v145
	v_rcp_iflag_f32_e32 v152, v112
	v_cvt_f32_ubyte3_e32 v112, v144
	v_rcp_iflag_f32_e32 v151, v112
	v_cvt_f32_ubyte3_e32 v112, v145
	v_rcp_iflag_f32_e32 v153, v112
	v_cvt_f32_ubyte1_e32 v157, v140
	v_cvt_f32_ubyte0_e32 v156, v140
	v_pk_mul_f32 v[114:115], v[114:115], v[156:157]
	v_cvt_f32_ubyte1_e32 v145, v141
	v_pk_mul_f32 v[28:29], v[28:29], v[114:115]
	v_cvt_f32_ubyte3_e32 v115, v141
	v_cvt_f32_ubyte2_e32 v114, v141
	v_cvt_f32_ubyte0_e32 v144, v141
	v_pk_mul_f32 v[114:115], v[152:153], v[114:115]
	v_cvt_f32_ubyte0_e32 v112, v146
	v_cvt_f32_ubyte3_e32 v155, v140
	v_cvt_f32_ubyte2_e32 v154, v140
	v_pk_mul_f32 v[140:141], v[148:149], v[144:145]
	v_pk_mul_f32 v[26:27], v[26:27], v[114:115]
	v_rcp_iflag_f32_e32 v114, v112
	v_cvt_f32_ubyte0_e32 v112, v147
	v_pk_mul_f32 v[24:25], v[24:25], v[140:141]
	v_rcp_iflag_f32_e32 v140, v112
	v_cvt_f32_ubyte1_e32 v112, v146
	v_rcp_iflag_f32_e32 v115, v112
	v_cvt_f32_ubyte1_e32 v112, v147
	v_rcp_iflag_f32_e32 v141, v112
	v_cvt_f32_ubyte2_e32 v112, v146
	v_rcp_iflag_f32_e32 v144, v112
	v_cvt_f32_ubyte2_e32 v112, v147
	v_rcp_iflag_f32_e32 v148, v112
	v_cvt_f32_ubyte3_e32 v112, v146
	v_rcp_iflag_f32_e32 v145, v112
	v_cvt_f32_ubyte3_e32 v112, v147
	v_rcp_iflag_f32_e32 v149, v112
	v_pk_mul_f32 v[150:151], v[150:151], v[154:155]
	v_cvt_f32_ubyte1_e32 v153, v142
	v_cvt_f32_ubyte0_e32 v152, v142
	v_pk_mul_f32 v[30:31], v[30:31], v[150:151]
	v_cvt_f32_ubyte3_e32 v151, v142
	v_cvt_f32_ubyte2_e32 v150, v142
	v_pk_mul_f32 v[114:115], v[114:115], v[152:153]
	v_pk_mul_f32 v[144:145], v[144:145], v[150:151]
	v_pk_mul_f32 v[20:21], v[20:21], v[114:115]
	v_cvt_f32_ubyte3_e32 v115, v143
	v_cvt_f32_ubyte2_e32 v114, v143
	v_pk_mul_f32 v[22:23], v[22:23], v[144:145]
	v_cvt_f32_ubyte1_e32 v145, v143
	v_cvt_f32_ubyte0_e32 v144, v143
	v_pk_mul_f32 v[114:115], v[148:149], v[114:115]
	s_waitcnt vmcnt(0)
	v_cvt_f32_ubyte0_e32 v112, v136
	v_pk_mul_f32 v[140:141], v[140:141], v[144:145]
	v_pk_mul_f32 v[18:19], v[18:19], v[114:115]
	v_rcp_iflag_f32_e32 v114, v112
	v_cvt_f32_ubyte0_e32 v112, v137
	v_pk_mul_f32 v[16:17], v[16:17], v[140:141]
	v_rcp_iflag_f32_e32 v140, v112
	v_cvt_f32_ubyte1_e32 v112, v136
	v_rcp_iflag_f32_e32 v115, v112
	v_cvt_f32_ubyte1_e32 v112, v137
	v_rcp_iflag_f32_e32 v141, v112
	v_cvt_f32_ubyte2_e32 v112, v136
	v_rcp_iflag_f32_e32 v142, v112
	v_cvt_f32_ubyte2_e32 v112, v137
	v_rcp_iflag_f32_e32 v144, v112
	v_cvt_f32_ubyte3_e32 v112, v136
	v_rcp_iflag_f32_e32 v143, v112
	v_cvt_f32_ubyte3_e32 v112, v137
	v_rcp_iflag_f32_e32 v145, v112
	v_cvt_f32_ubyte1_e32 v149, v132
	v_cvt_f32_ubyte0_e32 v148, v132
	v_pk_mul_f32 v[114:115], v[114:115], v[148:149]
	v_cvt_f32_ubyte1_e32 v137, v133
	v_pk_mul_f32 v[12:13], v[12:13], v[114:115]
	v_cvt_f32_ubyte3_e32 v115, v133
	v_cvt_f32_ubyte2_e32 v114, v133
	v_cvt_f32_ubyte0_e32 v136, v133
	v_pk_mul_f32 v[114:115], v[144:145], v[114:115]
	v_cvt_f32_ubyte0_e32 v112, v138
	v_cvt_f32_ubyte3_e32 v147, v132
	v_cvt_f32_ubyte2_e32 v146, v132
	v_pk_mul_f32 v[132:133], v[140:141], v[136:137]
	v_pk_mul_f32 v[10:11], v[10:11], v[114:115]
	v_rcp_iflag_f32_e32 v114, v112
	v_cvt_f32_ubyte0_e32 v112, v139
	v_pk_mul_f32 v[8:9], v[8:9], v[132:133]
	v_rcp_iflag_f32_e32 v132, v112
	v_cvt_f32_ubyte1_e32 v112, v138
	v_rcp_iflag_f32_e32 v115, v112
	v_cvt_f32_ubyte1_e32 v112, v139
	v_rcp_iflag_f32_e32 v133, v112
	v_cvt_f32_ubyte2_e32 v112, v138
	v_rcp_iflag_f32_e32 v136, v112
	v_cvt_f32_ubyte2_e32 v112, v139
	v_rcp_iflag_f32_e32 v140, v112
	v_cvt_f32_ubyte3_e32 v112, v138
	v_rcp_iflag_f32_e32 v137, v112
	v_cvt_f32_ubyte3_e32 v112, v139
	v_pk_mul_f32 v[142:143], v[142:143], v[146:147]
	v_rcp_iflag_f32_e32 v141, v112
	v_pk_mul_f32 v[14:15], v[14:15], v[142:143]
	v_cvt_f32_ubyte3_e32 v143, v134
	v_cvt_f32_ubyte2_e32 v142, v134
	v_cvt_f32_ubyte1_e32 v145, v134
	v_cvt_f32_ubyte0_e32 v144, v134
	v_pk_mul_f32 v[114:115], v[114:115], v[144:145]
	v_pk_mul_f32 v[136:137], v[136:137], v[142:143]
	v_pk_mul_f32 v[4:5], v[4:5], v[114:115]
	v_pk_mul_f32 v[6:7], v[6:7], v[136:137]
	v_cvt_f32_ubyte3_e32 v115, v135
	v_cvt_f32_ubyte2_e32 v114, v135
	v_cvt_f32_ubyte1_e32 v137, v135
	v_cvt_f32_ubyte0_e32 v136, v135
	v_pk_mul_f32 v[132:133], v[132:133], v[136:137]
	v_pk_mul_f32 v[114:115], v[140:141], v[114:115]
	v_pk_mul_f32 v[0:1], v[0:1], v[132:133]
	v_pk_mul_f32 v[2:3], v[2:3], v[114:115]
	s_mov_b32 s30, s1
	s_and_b64 vcc, exec, s[40:41]
	s_mov_b64 s[40:41], -1
	s_cbranch_vccnz .LBB0_742
